# speedup vs baseline: 1.0101x; 1.0101x over previous
attn_fwd_pwg4x64:
	s_load_dwordx2 s[22:23], s[0:1], 0x0
	s_load_dwordx8 s[4:11], s[0:1], 0x8
	s_load_dwordx2 s[36:37], s[0:1], 0x28
	s_load_dwordx4 s[16:19], s[0:1], 0x30
	s_load_dwordx2 s[20:21], s[0:1], 0x40
	s_and_b32 s3, s2, 15
	s_bfe_u32 s30, s2, 0x30004
	s_lshr_b32 s2, s2, 3
	s_and_b32 s2, s2, 0x1ffffff0
	s_or_b32 s2, s2, s3
	s_mov_b32 s3, 0
	s_lshl_b32 s31, s30, 8
	s_lshl_b64 s[26:27], s[2:3], 19
	s_lshl_b64 s[24:25], s[2:3], 11
	s_lshl_b64 s[38:39], s[2:3], 20
	s_lshl_b32 s43, s30, 17
	s_add_u32 s38, s38, s43
	s_addc_u32 s39, s39, 0
	v_and_b32_e32 v1, 15, v0
	v_lshrrev_b32_e32 v28, 4, v0
	v_lshrrev_b32_e32 v29, 6, v0
	v_lshlrev_b32_e32 v30, 5, v1
	v_lshl_or_b32 v2, v28, 9, v30
	v_bfe_u32 v31, v0, 4, 2
	v_lshl_or_b32 v3, v31, 9, v30
	v_lshl_or_b32 v3, v29, 15, v3
	v_lshlrev_b32_e32 v32, 4, v1
	v_lshl_or_b32 v26, v28, 8, v32
	s_lshl_b32 s43, s30, 16
	v_or_b32_e32 v26, s43, v26
	v_lshlrev_b32_e32 v38, 2, v0
	v_lshlrev_b32_e32 v40, 14, v29
	v_lshlrev_b32_e32 v33, 12, v29
	v_mbcnt_lo_u32_b32 v204, -1, 0
	v_mbcnt_hi_u32_b32 v204, -1, v204
	v_readfirstlane_b32 s28, v33
	v_readfirstlane_b32 s29, v33
	v_mov_b32_e32 v4, 0
	v_mov_b32_e32 v5, 0
	v_mov_b32_e32 v6, 0
	v_mov_b32_e32 v7, 0
	v_mov_b32_e32 v8, 0
	v_mov_b32_e32 v9, 0
	v_mov_b32_e32 v10, 0
	v_mov_b32_e32 v11, 0
	s_mov_b32 s44, 0x3e0293ee
	s_mov_b32 s45, 0x3e0293ee
	s_waitcnt lgkmcnt(0)
	s_add_u32 s12, s4, s26
	s_addc_u32 s13, s5, s27
	s_and_b32 s13, s13, 0xffff
	s_mov_b32 s14, 0x80000
	s_mov_b32 s15, 0x20000
	s_add_u32 s4, s6, s26
	s_addc_u32 s5, s7, s27
	s_and_b32 s5, s5, 0xffff
	s_mov_b32 s6, 0x80000
	s_mov_b32 s7, 0x20000
	s_add_u32 s32, s10, s38
	s_addc_u32 s33, s11, s39
	s_add_u32 s34, s36, s38
	s_addc_u32 s35, s37, s39
	s_add_u32 s40, s22, s38
	s_addc_u32 s41, s23, s39
	s_lshl_b64 s[46:47], s[2:3], 5
	s_add_u32 s10, s16, s46
	s_addc_u32 s11, s17, s47
	s_lshl_b32 s43, s30, 2
	s_add_u32 s46, s10, s43
	s_addc_u32 s47, s11, 0
	s_lshl_b64 s[26:27], s[2:3], 12
	s_add_u32 s26, s18, s26
	s_addc_u32 s27, s19, s27
	s_lshl_b32 s43, s30, 9
	s_add_u32 s26, s26, s43
	s_addc_u32 s27, s27, 0
	global_load_dwordx4 v[42:45], v2, s[32:33] nt
	global_load_dwordx4 v[46:49], v2, s[32:33] offset:16 nt
	s_add_u32 s32, s32, 8192
	s_addc_u32 s33, s33, 0
	global_load_dwordx4 v[50:53], v2, s[32:33] nt
	global_load_dwordx4 v[54:57], v2, s[32:33] offset:16 nt
	s_add_u32 s32, s32, 8192
	s_addc_u32 s33, s33, 0
	global_load_dwordx4 v[58:61], v2, s[32:33] nt
	global_load_dwordx4 v[62:65], v2, s[32:33] offset:16 nt
	s_add_u32 s32, s32, 8192
	s_addc_u32 s33, s33, 0
	global_load_dwordx4 v[66:69], v2, s[32:33] nt
	global_load_dwordx4 v[70:73], v2, s[32:33] offset:16 nt
	s_add_u32 s32, s32, 8192
	s_addc_u32 s33, s33, 0
	global_load_dwordx4 v[74:77], v2, s[32:33] nt
	global_load_dwordx4 v[78:81], v2, s[32:33] offset:16 nt
	s_add_u32 s32, s32, 8192
	s_addc_u32 s33, s33, 0
	global_load_dwordx4 v[82:85], v2, s[32:33] nt
	global_load_dwordx4 v[86:89], v2, s[32:33] offset:16 nt
	s_add_u32 s32, s32, 8192
	s_addc_u32 s33, s33, 0
	global_load_dwordx4 v[90:93], v2, s[32:33] nt
	global_load_dwordx4 v[94:97], v2, s[32:33] offset:16 nt
	s_add_u32 s32, s32, 8192
	s_addc_u32 s33, s33, 0
	global_load_dwordx4 v[98:101], v2, s[32:33] nt
	global_load_dwordx4 v[102:105], v2, s[32:33] offset:16 nt
	s_add_u32 s32, s32, 8192
	s_addc_u32 s33, s33, 0
	global_load_dwordx4 v[106:109], v2, s[32:33] nt
	global_load_dwordx4 v[110:113], v2, s[32:33] offset:16 nt
	s_add_u32 s32, s32, 8192
	s_addc_u32 s33, s33, 0
	global_load_dwordx4 v[114:117], v2, s[32:33] nt
	global_load_dwordx4 v[118:121], v2, s[32:33] offset:16 nt
	s_add_u32 s32, s32, 8192
	s_addc_u32 s33, s33, 0
	global_load_dwordx4 v[122:125], v2, s[32:33] nt
	global_load_dwordx4 v[126:129], v2, s[32:33] offset:16 nt
	s_add_u32 s32, s32, 8192
	s_addc_u32 s33, s33, 0
	global_load_dwordx4 v[130:133], v2, s[32:33] nt
	global_load_dwordx4 v[134:137], v2, s[32:33] offset:16 nt
	s_add_u32 s32, s32, 8192
	s_addc_u32 s33, s33, 0
	global_load_dwordx4 v[138:141], v2, s[32:33] nt
	global_load_dwordx4 v[142:145], v2, s[32:33] offset:16 nt
	s_add_u32 s32, s32, 8192
	s_addc_u32 s33, s33, 0
	global_load_dwordx4 v[146:149], v2, s[32:33] nt
	global_load_dwordx4 v[150:153], v2, s[32:33] offset:16 nt
	s_add_u32 s32, s32, 8192
	s_addc_u32 s33, s33, 0
	global_load_dwordx4 v[154:157], v2, s[32:33] nt
	global_load_dwordx4 v[158:161], v2, s[32:33] offset:16 nt
	s_add_u32 s32, s32, 8192
	s_addc_u32 s33, s33, 0
	global_load_dwordx4 v[162:165], v2, s[32:33] nt
	global_load_dwordx4 v[166:169], v2, s[32:33] offset:16 nt
	s_add_u32 s32, s32, 8192
	s_addc_u32 s33, s33, 0
	global_load_dwordx4 v[170:173], v2, s[34:35] nt
	global_load_dwordx4 v[174:177], v2, s[34:35] offset:16 nt
	s_add_u32 s34, s34, 8192
	s_addc_u32 s35, s35, 0
	global_load_dwordx4 v[178:181], v2, s[34:35] nt
	global_load_dwordx4 v[182:185], v2, s[34:35] offset:16 nt
	s_add_u32 s34, s34, 8192
	s_addc_u32 s35, s35, 0
	global_load_dwordx4 v[186:189], v2, s[34:35] nt
	global_load_dwordx4 v[190:193], v2, s[34:35] offset:16 nt
	s_add_u32 s34, s34, 8192
	s_addc_u32 s35, s35, 0
	global_load_dwordx4 v[194:197], v2, s[34:35] nt
	global_load_dwordx4 v[198:201], v2, s[34:35] offset:16 nt
	s_add_u32 s34, s34, 8192
	s_addc_u32 s35, s35, 0
	s_waitcnt vmcnt(38)
	v_cvt_pk_bf16_f32 v12, v42, v43
	v_cvt_pk_bf16_f32 v13, v44, v45
	v_cvt_pk_bf16_f32 v14, v46, v47
	v_cvt_pk_bf16_f32 v15, v48, v49
	s_mov_b32 s42, 0x0
	buffer_store_dwordx4 v[12:15], v26, s[12:15], s42 offen sc1
	global_load_dwordx4 v[42:45], v2, s[34:35] nt
	global_load_dwordx4 v[46:49], v2, s[34:35] offset:16 nt
	s_add_u32 s34, s34, 8192
	s_addc_u32 s35, s35, 0
	s_waitcnt vmcnt(39)
	v_cvt_pk_bf16_f32 v16, v50, v51
	v_cvt_pk_bf16_f32 v17, v52, v53
	v_cvt_pk_bf16_f32 v18, v54, v55
	v_cvt_pk_bf16_f32 v19, v56, v57
	s_mov_b32 s42, 0x1000
	buffer_store_dwordx4 v[16:19], v26, s[12:15], s42 offen sc1
	global_load_dwordx4 v[50:53], v2, s[34:35] nt
	global_load_dwordx4 v[54:57], v2, s[34:35] offset:16 nt
	s_add_u32 s34, s34, 8192
	s_addc_u32 s35, s35, 0
	s_waitcnt vmcnt(40)
	v_cvt_pk_bf16_f32 v20, v58, v59
	v_cvt_pk_bf16_f32 v21, v60, v61
	v_cvt_pk_bf16_f32 v22, v62, v63
	v_cvt_pk_bf16_f32 v23, v64, v65
	s_mov_b32 s42, 0x2000
	buffer_store_dwordx4 v[20:23], v26, s[12:15], s42 offen sc1
	global_load_dwordx4 v[58:61], v2, s[34:35] nt
	global_load_dwordx4 v[62:65], v2, s[34:35] offset:16 nt
	s_add_u32 s34, s34, 8192
	s_addc_u32 s35, s35, 0
	s_waitcnt vmcnt(41)
	v_cvt_pk_bf16_f32 v12, v66, v67
	v_cvt_pk_bf16_f32 v13, v68, v69
	v_cvt_pk_bf16_f32 v14, v70, v71
	v_cvt_pk_bf16_f32 v15, v72, v73
	s_mov_b32 s42, 0x3000
	buffer_store_dwordx4 v[12:15], v26, s[12:15], s42 offen sc1
	global_load_dwordx4 v[66:69], v2, s[34:35] nt
	global_load_dwordx4 v[70:73], v2, s[34:35] offset:16 nt
	s_add_u32 s34, s34, 8192
	s_addc_u32 s35, s35, 0
	s_waitcnt vmcnt(42)
	v_cvt_pk_bf16_f32 v16, v74, v75
	v_cvt_pk_bf16_f32 v17, v76, v77
	v_cvt_pk_bf16_f32 v18, v78, v79
	v_cvt_pk_bf16_f32 v19, v80, v81
	s_mov_b32 s42, 0x4000
	buffer_store_dwordx4 v[16:19], v26, s[12:15], s42 offen sc1
	global_load_dwordx4 v[74:77], v2, s[34:35] nt
	global_load_dwordx4 v[78:81], v2, s[34:35] offset:16 nt
	s_add_u32 s34, s34, 8192
	s_addc_u32 s35, s35, 0
	s_waitcnt vmcnt(43)
	v_cvt_pk_bf16_f32 v20, v82, v83
	v_cvt_pk_bf16_f32 v21, v84, v85
	v_cvt_pk_bf16_f32 v22, v86, v87
	v_cvt_pk_bf16_f32 v23, v88, v89
	s_mov_b32 s42, 0x5000
	buffer_store_dwordx4 v[20:23], v26, s[12:15], s42 offen sc1
	global_load_dwordx4 v[82:85], v2, s[34:35] nt
	global_load_dwordx4 v[86:89], v2, s[34:35] offset:16 nt
	s_add_u32 s34, s34, 8192
	s_addc_u32 s35, s35, 0
	s_waitcnt vmcnt(44)
	v_cvt_pk_bf16_f32 v12, v90, v91
	v_cvt_pk_bf16_f32 v13, v92, v93
	v_cvt_pk_bf16_f32 v14, v94, v95
	v_cvt_pk_bf16_f32 v15, v96, v97
	s_mov_b32 s42, 0x6000
	buffer_store_dwordx4 v[12:15], v26, s[12:15], s42 offen sc1
	global_load_dwordx4 v[90:93], v2, s[34:35] nt
	global_load_dwordx4 v[94:97], v2, s[34:35] offset:16 nt
	s_add_u32 s34, s34, 8192
	s_addc_u32 s35, s35, 0
	s_waitcnt vmcnt(45)
	v_cvt_pk_bf16_f32 v16, v98, v99
	v_cvt_pk_bf16_f32 v17, v100, v101
	v_cvt_pk_bf16_f32 v18, v102, v103
	v_cvt_pk_bf16_f32 v19, v104, v105
	s_mov_b32 s42, 0x7000
	buffer_store_dwordx4 v[16:19], v26, s[12:15], s42 offen sc1
	global_load_dwordx4 v[98:101], v2, s[34:35] nt
	global_load_dwordx4 v[102:105], v2, s[34:35] offset:16 nt
	s_add_u32 s34, s34, 8192
	s_addc_u32 s35, s35, 0
	s_waitcnt vmcnt(46)
	v_cvt_pk_bf16_f32 v20, v106, v107
	v_cvt_pk_bf16_f32 v21, v108, v109
	v_cvt_pk_bf16_f32 v22, v110, v111
	v_cvt_pk_bf16_f32 v23, v112, v113
	s_mov_b32 s42, 0x8000
	buffer_store_dwordx4 v[20:23], v26, s[12:15], s42 offen sc1
	global_load_dwordx4 v[106:109], v2, s[34:35] nt
	global_load_dwordx4 v[110:113], v2, s[34:35] offset:16 nt
	s_add_u32 s34, s34, 8192
	s_addc_u32 s35, s35, 0
	s_waitcnt vmcnt(47)
	v_cvt_pk_bf16_f32 v12, v114, v115
	v_cvt_pk_bf16_f32 v13, v116, v117
	v_cvt_pk_bf16_f32 v14, v118, v119
	v_cvt_pk_bf16_f32 v15, v120, v121
	s_mov_b32 s42, 0x9000
	buffer_store_dwordx4 v[12:15], v26, s[12:15], s42 offen sc1
	global_load_dwordx4 v[114:117], v2, s[34:35] nt
	global_load_dwordx4 v[118:121], v2, s[34:35] offset:16 nt
	s_add_u32 s34, s34, 8192
	s_addc_u32 s35, s35, 0
	s_waitcnt vmcnt(48)
	v_cvt_pk_bf16_f32 v16, v122, v123
	v_cvt_pk_bf16_f32 v17, v124, v125
	v_cvt_pk_bf16_f32 v18, v126, v127
	v_cvt_pk_bf16_f32 v19, v128, v129
	s_mov_b32 s42, 0xa000
	buffer_store_dwordx4 v[16:19], v26, s[12:15], s42 offen sc1
	global_load_dwordx4 v[122:125], v2, s[34:35] nt
	global_load_dwordx4 v[126:129], v2, s[34:35] offset:16 nt
	s_add_u32 s34, s34, 8192
	s_addc_u32 s35, s35, 0
	s_waitcnt vmcnt(49)
	v_cvt_pk_bf16_f32 v20, v130, v131
	v_cvt_pk_bf16_f32 v21, v132, v133
	v_cvt_pk_bf16_f32 v22, v134, v135
	v_cvt_pk_bf16_f32 v23, v136, v137
	s_mov_b32 s42, 0xb000
	buffer_store_dwordx4 v[20:23], v26, s[12:15], s42 offen sc1
	global_load_dwordx4 v[130:133], v2, s[34:35] nt
	global_load_dwordx4 v[134:137], v2, s[34:35] offset:16 nt
	s_add_u32 s34, s34, 8192
	s_addc_u32 s35, s35, 0
	s_waitcnt vmcnt(50)
	v_cvt_pk_bf16_f32 v12, v138, v139
	v_cvt_pk_bf16_f32 v13, v140, v141
	v_cvt_pk_bf16_f32 v14, v142, v143
	v_cvt_pk_bf16_f32 v15, v144, v145
	s_mov_b32 s42, 0xc000
	buffer_store_dwordx4 v[12:15], v26, s[12:15], s42 offen sc1
	global_load_dwordx4 v[138:141], v3, s[40:41] nt
	global_load_dwordx4 v[142:145], v3, s[40:41] offset:16 nt
	s_add_u32 s40, s40, 2048
	s_addc_u32 s41, s41, 0
	s_waitcnt vmcnt(51)
	v_cvt_pk_bf16_f32 v16, v146, v147
	v_cvt_pk_bf16_f32 v17, v148, v149
	v_cvt_pk_bf16_f32 v18, v150, v151
	v_cvt_pk_bf16_f32 v19, v152, v153
	s_mov_b32 s42, 0xd000
	buffer_store_dwordx4 v[16:19], v26, s[12:15], s42 offen sc1
	global_load_dwordx4 v[146:149], v3, s[40:41] nt
	global_load_dwordx4 v[150:153], v3, s[40:41] offset:16 nt
	s_add_u32 s40, s40, 2048
	s_addc_u32 s41, s41, 0
	s_waitcnt vmcnt(52)
	v_cvt_pk_bf16_f32 v20, v154, v155
	v_cvt_pk_bf16_f32 v21, v156, v157
	v_cvt_pk_bf16_f32 v22, v158, v159
	v_cvt_pk_bf16_f32 v23, v160, v161
	s_mov_b32 s42, 0xe000
	buffer_store_dwordx4 v[20:23], v26, s[12:15], s42 offen sc1
	global_load_dwordx4 v[154:157], v3, s[40:41] nt
	global_load_dwordx4 v[158:161], v3, s[40:41] offset:16 nt
	s_add_u32 s40, s40, 2048
	s_addc_u32 s41, s41, 0
	s_waitcnt vmcnt(53)
	v_cvt_pk_bf16_f32 v12, v162, v163
	v_cvt_pk_bf16_f32 v13, v164, v165
	v_cvt_pk_bf16_f32 v14, v166, v167
	v_cvt_pk_bf16_f32 v15, v168, v169
	s_mov_b32 s42, 0xf000
	buffer_store_dwordx4 v[12:15], v26, s[12:15], s42 offen sc1
	global_load_dwordx4 v[162:165], v3, s[40:41] nt
	global_load_dwordx4 v[166:169], v3, s[40:41] offset:16 nt
	s_add_u32 s40, s40, 2048
	s_addc_u32 s41, s41, 0
	s_waitcnt vmcnt(54)
	v_pk_add_f32 v[4:5], v[170:171], v[4:5]
	v_pk_add_f32 v[6:7], v[172:173], v[6:7]
	v_pk_add_f32 v[8:9], v[174:175], v[8:9]
	v_pk_add_f32 v[10:11], v[176:177], v[10:11]
	v_cvt_pk_bf16_f32 v16, v170, v171
	v_cvt_pk_bf16_f32 v17, v172, v173
	v_cvt_pk_bf16_f32 v18, v174, v175
	v_cvt_pk_bf16_f32 v19, v176, v177
	s_mov_b32 s42, 0x0
	buffer_store_dwordx4 v[16:19], v26, s[4:7], s42 offen sc1
	global_load_dwordx4 v[170:173], v3, s[40:41] nt
	global_load_dwordx4 v[174:177], v3, s[40:41] offset:16 nt
	s_add_u32 s40, s40, 2048
	s_addc_u32 s41, s41, 0
	s_waitcnt vmcnt(55)
	v_pk_add_f32 v[4:5], v[178:179], v[4:5]
	v_pk_add_f32 v[6:7], v[180:181], v[6:7]
	v_pk_add_f32 v[8:9], v[182:183], v[8:9]
	v_pk_add_f32 v[10:11], v[184:185], v[10:11]
	v_cvt_pk_bf16_f32 v20, v178, v179
	v_cvt_pk_bf16_f32 v21, v180, v181
	v_cvt_pk_bf16_f32 v22, v182, v183
	v_cvt_pk_bf16_f32 v23, v184, v185
	s_mov_b32 s42, 0x1000
	buffer_store_dwordx4 v[20:23], v26, s[4:7], s42 offen sc1
	global_load_dwordx4 v[178:181], v3, s[40:41] nt
	global_load_dwordx4 v[182:185], v3, s[40:41] offset:16 nt
	s_add_u32 s40, s40, 2048
	s_addc_u32 s41, s41, 0
	s_waitcnt vmcnt(56)
	v_pk_add_f32 v[4:5], v[186:187], v[4:5]
	v_pk_add_f32 v[6:7], v[188:189], v[6:7]
	v_pk_add_f32 v[8:9], v[190:191], v[8:9]
	v_pk_add_f32 v[10:11], v[192:193], v[10:11]
	v_cvt_pk_bf16_f32 v12, v186, v187
	v_cvt_pk_bf16_f32 v13, v188, v189
	v_cvt_pk_bf16_f32 v14, v190, v191
	v_cvt_pk_bf16_f32 v15, v192, v193
	s_mov_b32 s42, 0x2000
	buffer_store_dwordx4 v[12:15], v26, s[4:7], s42 offen sc1
	global_load_dwordx4 v[186:189], v3, s[40:41] nt
	global_load_dwordx4 v[190:193], v3, s[40:41] offset:16 nt
	s_add_u32 s40, s40, 2048
	s_addc_u32 s41, s41, 0
	s_waitcnt vmcnt(57)
	v_pk_add_f32 v[4:5], v[194:195], v[4:5]
	v_pk_add_f32 v[6:7], v[196:197], v[6:7]
	v_pk_add_f32 v[8:9], v[198:199], v[8:9]
	v_pk_add_f32 v[10:11], v[200:201], v[10:11]
	v_cvt_pk_bf16_f32 v16, v194, v195
	v_cvt_pk_bf16_f32 v17, v196, v197
	v_cvt_pk_bf16_f32 v18, v198, v199
	v_cvt_pk_bf16_f32 v19, v200, v201
	s_mov_b32 s42, 0x3000
	buffer_store_dwordx4 v[16:19], v26, s[4:7], s42 offen sc1
	global_load_dwordx4 v[194:197], v3, s[40:41] nt
	global_load_dwordx4 v[198:201], v3, s[40:41] offset:16 nt
	s_add_u32 s40, s40, 2048
	s_addc_u32 s41, s41, 0
	s_waitcnt vmcnt(57)
	v_pk_add_f32 v[4:5], v[42:43], v[4:5]
	v_pk_add_f32 v[6:7], v[44:45], v[6:7]
	v_pk_add_f32 v[8:9], v[46:47], v[8:9]
	v_pk_add_f32 v[10:11], v[48:49], v[10:11]
	v_cvt_pk_bf16_f32 v20, v42, v43
	v_cvt_pk_bf16_f32 v21, v44, v45
	v_cvt_pk_bf16_f32 v22, v46, v47
	v_cvt_pk_bf16_f32 v23, v48, v49
	s_mov_b32 s42, 0x4000
	buffer_store_dwordx4 v[20:23], v26, s[4:7], s42 offen sc1
	global_load_dwordx4 v[42:45], v3, s[40:41] nt
	global_load_dwordx4 v[46:49], v3, s[40:41] offset:16 nt
	s_add_u32 s40, s40, 2048
	s_addc_u32 s41, s41, 0
	s_waitcnt vmcnt(57)
	v_pk_add_f32 v[4:5], v[50:51], v[4:5]
	v_pk_add_f32 v[6:7], v[52:53], v[6:7]
	v_pk_add_f32 v[8:9], v[54:55], v[8:9]
	v_pk_add_f32 v[10:11], v[56:57], v[10:11]
	v_cvt_pk_bf16_f32 v12, v50, v51
	v_cvt_pk_bf16_f32 v13, v52, v53
	v_cvt_pk_bf16_f32 v14, v54, v55
	v_cvt_pk_bf16_f32 v15, v56, v57
	s_mov_b32 s42, 0x5000
	buffer_store_dwordx4 v[12:15], v26, s[4:7], s42 offen sc1
	global_load_dwordx4 v[50:53], v3, s[40:41] nt
	global_load_dwordx4 v[54:57], v3, s[40:41] offset:16 nt
	s_add_u32 s40, s40, 2048
	s_addc_u32 s41, s41, 0
	s_waitcnt vmcnt(57)
	v_pk_add_f32 v[4:5], v[58:59], v[4:5]
	v_pk_add_f32 v[6:7], v[60:61], v[6:7]
	v_pk_add_f32 v[8:9], v[62:63], v[8:9]
	v_pk_add_f32 v[10:11], v[64:65], v[10:11]
	v_cvt_pk_bf16_f32 v16, v58, v59
	v_cvt_pk_bf16_f32 v17, v60, v61
	v_cvt_pk_bf16_f32 v18, v62, v63
	v_cvt_pk_bf16_f32 v19, v64, v65
	s_mov_b32 s42, 0x6000
	buffer_store_dwordx4 v[16:19], v26, s[4:7], s42 offen sc1
	global_load_dwordx4 v[58:61], v3, s[40:41] nt
	global_load_dwordx4 v[62:65], v3, s[40:41] offset:16 nt
	s_add_u32 s40, s40, 2048
	s_addc_u32 s41, s41, 0
	s_waitcnt vmcnt(57)
	v_pk_add_f32 v[4:5], v[66:67], v[4:5]
	v_pk_add_f32 v[6:7], v[68:69], v[6:7]
	v_pk_add_f32 v[8:9], v[70:71], v[8:9]
	v_pk_add_f32 v[10:11], v[72:73], v[10:11]
	v_cvt_pk_bf16_f32 v20, v66, v67
	v_cvt_pk_bf16_f32 v21, v68, v69
	v_cvt_pk_bf16_f32 v22, v70, v71
	v_cvt_pk_bf16_f32 v23, v72, v73
	s_mov_b32 s42, 0x7000
	buffer_store_dwordx4 v[20:23], v26, s[4:7], s42 offen sc1
	global_load_dwordx4 v[66:69], v3, s[40:41] nt
	global_load_dwordx4 v[70:73], v3, s[40:41] offset:16 nt
	s_add_u32 s40, s40, 2048
	s_addc_u32 s41, s41, 0
	s_waitcnt vmcnt(57)
	v_pk_add_f32 v[4:5], v[74:75], v[4:5]
	v_pk_add_f32 v[6:7], v[76:77], v[6:7]
	v_pk_add_f32 v[8:9], v[78:79], v[8:9]
	v_pk_add_f32 v[10:11], v[80:81], v[10:11]
	v_cvt_pk_bf16_f32 v12, v74, v75
	v_cvt_pk_bf16_f32 v13, v76, v77
	v_cvt_pk_bf16_f32 v14, v78, v79
	v_cvt_pk_bf16_f32 v15, v80, v81
	s_mov_b32 s42, 0x8000
	buffer_store_dwordx4 v[12:15], v26, s[4:7], s42 offen sc1
	global_load_dwordx4 v[74:77], v3, s[40:41] nt
	global_load_dwordx4 v[78:81], v3, s[40:41] offset:16 nt
	s_add_u32 s40, s40, 2048
	s_addc_u32 s41, s41, 0
	s_waitcnt vmcnt(57)
	v_pk_add_f32 v[4:5], v[82:83], v[4:5]
	v_pk_add_f32 v[6:7], v[84:85], v[6:7]
	v_pk_add_f32 v[8:9], v[86:87], v[8:9]
	v_pk_add_f32 v[10:11], v[88:89], v[10:11]
	v_cvt_pk_bf16_f32 v16, v82, v83
	v_cvt_pk_bf16_f32 v17, v84, v85
	v_cvt_pk_bf16_f32 v18, v86, v87
	v_cvt_pk_bf16_f32 v19, v88, v89
	s_mov_b32 s42, 0x9000
	buffer_store_dwordx4 v[16:19], v26, s[4:7], s42 offen sc1
	global_load_dwordx4 v[82:85], v3, s[40:41] nt
	global_load_dwordx4 v[86:89], v3, s[40:41] offset:16 nt
	s_add_u32 s40, s40, 2048
	s_addc_u32 s41, s41, 0
	s_waitcnt vmcnt(57)
	v_pk_add_f32 v[4:5], v[90:91], v[4:5]
	v_pk_add_f32 v[6:7], v[92:93], v[6:7]
	v_pk_add_f32 v[8:9], v[94:95], v[8:9]
	v_pk_add_f32 v[10:11], v[96:97], v[10:11]
	v_cvt_pk_bf16_f32 v20, v90, v91
	v_cvt_pk_bf16_f32 v21, v92, v93
	v_cvt_pk_bf16_f32 v22, v94, v95
	v_cvt_pk_bf16_f32 v23, v96, v97
	s_mov_b32 s42, 0xa000
	buffer_store_dwordx4 v[20:23], v26, s[4:7], s42 offen sc1
	global_load_dwordx4 v[90:93], v3, s[40:41] nt
	global_load_dwordx4 v[94:97], v3, s[40:41] offset:16 nt
	s_add_u32 s40, s40, 2048
	s_addc_u32 s41, s41, 0
	s_waitcnt vmcnt(57)
	v_pk_add_f32 v[4:5], v[98:99], v[4:5]
	v_pk_add_f32 v[6:7], v[100:101], v[6:7]
	v_pk_add_f32 v[8:9], v[102:103], v[8:9]
	v_pk_add_f32 v[10:11], v[104:105], v[10:11]
	v_cvt_pk_bf16_f32 v12, v98, v99
	v_cvt_pk_bf16_f32 v13, v100, v101
	v_cvt_pk_bf16_f32 v14, v102, v103
	v_cvt_pk_bf16_f32 v15, v104, v105
	s_mov_b32 s42, 0xb000
	buffer_store_dwordx4 v[12:15], v26, s[4:7], s42 offen sc1
	global_load_dwordx4 v[98:101], v3, s[40:41] nt
	global_load_dwordx4 v[102:105], v3, s[40:41] offset:16 nt
	s_add_u32 s40, s40, 2048
	s_addc_u32 s41, s41, 0
	s_waitcnt vmcnt(57)
	v_pk_add_f32 v[4:5], v[106:107], v[4:5]
	v_pk_add_f32 v[6:7], v[108:109], v[6:7]
	v_pk_add_f32 v[8:9], v[110:111], v[8:9]
	v_pk_add_f32 v[10:11], v[112:113], v[10:11]
	v_cvt_pk_bf16_f32 v16, v106, v107
	v_cvt_pk_bf16_f32 v17, v108, v109
	v_cvt_pk_bf16_f32 v18, v110, v111
	v_cvt_pk_bf16_f32 v19, v112, v113
	s_mov_b32 s42, 0xc000
	buffer_store_dwordx4 v[16:19], v26, s[4:7], s42 offen sc1
	s_waitcnt vmcnt(55)
	v_pk_add_f32 v[4:5], v[114:115], v[4:5]
	v_pk_add_f32 v[6:7], v[116:117], v[6:7]
	v_pk_add_f32 v[8:9], v[118:119], v[8:9]
	v_pk_add_f32 v[10:11], v[120:121], v[10:11]
	v_cvt_pk_bf16_f32 v20, v114, v115
	v_cvt_pk_bf16_f32 v21, v116, v117
	v_cvt_pk_bf16_f32 v22, v118, v119
	v_cvt_pk_bf16_f32 v23, v120, v121
	s_mov_b32 s42, 0xd000
	buffer_store_dwordx4 v[20:23], v26, s[4:7], s42 offen sc1
	s_waitcnt vmcnt(53)
	v_pk_add_f32 v[4:5], v[122:123], v[4:5]
	v_pk_add_f32 v[6:7], v[124:125], v[6:7]
	v_pk_add_f32 v[8:9], v[126:127], v[8:9]
	v_pk_add_f32 v[10:11], v[128:129], v[10:11]
	v_cvt_pk_bf16_f32 v12, v122, v123
	v_cvt_pk_bf16_f32 v13, v124, v125
	v_cvt_pk_bf16_f32 v14, v126, v127
	v_cvt_pk_bf16_f32 v15, v128, v129
	s_mov_b32 s42, 0xe000
	buffer_store_dwordx4 v[12:15], v26, s[4:7], s42 offen sc1
	s_waitcnt vmcnt(51)
	v_pk_add_f32 v[4:5], v[130:131], v[4:5]
	v_pk_add_f32 v[6:7], v[132:133], v[6:7]
	v_pk_add_f32 v[8:9], v[134:135], v[8:9]
	v_pk_add_f32 v[10:11], v[136:137], v[10:11]
	v_cvt_pk_bf16_f32 v16, v130, v131
	v_cvt_pk_bf16_f32 v17, v132, v133
	v_cvt_pk_bf16_f32 v18, v134, v135
	v_cvt_pk_bf16_f32 v19, v136, v137
	s_mov_b32 s42, 0xf000
	buffer_store_dwordx4 v[16:19], v26, s[4:7], s42 offen sc1
	v_mul_u32_u24_e32 v27, 0x210, v28
	s_mov_b32 s43, 0x20000
	v_add3_u32 v27, s43, v27, v30
	ds_write_b128 v27, v[4:7]
	ds_write_b128 v27, v[8:11] offset:16
	s_movk_i32 s0, 0x80
	v_cmp_gt_u32_e64 s[0:1], s0, v0
	s_waitcnt lgkmcnt(0)
	s_barrier
	s_and_saveexec_b64 s[38:39], s[0:1]
	s_cbranch_execz .Lpro_nopart
	v_add_u32_e32 v28, 0x20000, v38
	ds_read2_b32 v[12:13], v28 offset1:132
	v_add_u32_e32 v29, 0x400, v28
	ds_read2_b32 v[14:15], v29 offset0:8 offset1:140
	v_add_u32_e32 v29, 0x800, v28
	ds_read2_b32 v[16:17], v29 offset0:16 offset1:148
	v_add_u32_e32 v29, 0xc00, v28
	ds_read2_b32 v[18:19], v29 offset0:24 offset1:156
	v_add_u32_e32 v29, 0x1000, v28
	ds_read2_b32 v[20:21], v29 offset0:32 offset1:164
	v_add_u32_e32 v29, 0x1400, v28
	ds_read2_b32 v[22:23], v29 offset0:40 offset1:172
	v_add_u32_e32 v29, 0x1800, v28
	ds_read2_b32 v[24:25], v29 offset0:48 offset1:180
	v_add_u32_e32 v29, 0x1c00, v28
	ds_read2_b32 v[26:27], v29 offset0:56 offset1:188
	s_waitcnt lgkmcnt(0)
	v_add_f32_e32 v4, 0, v12
	v_add_f32_e32 v4, v4, v13
	v_add_f32_e32 v4, v4, v14
	v_add_f32_e32 v4, v4, v15
	v_add_f32_e32 v4, v4, v16
	v_add_f32_e32 v4, v4, v17
	v_add_f32_e32 v4, v4, v18
	v_add_f32_e32 v4, v4, v19
	v_add_f32_e32 v4, v4, v20
	v_add_f32_e32 v4, v4, v21
	v_add_f32_e32 v4, v4, v22
	v_add_f32_e32 v4, v4, v23
	v_add_f32_e32 v4, v4, v24
	v_add_f32_e32 v4, v4, v25
	v_add_f32_e32 v4, v4, v26
	v_add_f32_e32 v4, v4, v27
	global_store_dword v38, v4, s[26:27] sc1
.Lpro_nopart:
	s_or_b64 exec, exec, s[38:39]
	s_waitcnt vmcnt(0)
	s_barrier
	v_cmp_eq_u32_e32 vcc, 0, v0
	s_and_saveexec_b64 s[38:39], vcc
	s_cbranch_execz .Lpro_noflag
	v_mov_b32_e32 v12, 0x600df1a6
	v_mov_b32_e32 v13, 0
	global_store_dword v13, v12, s[46:47] sc1
.Lpro_noflag:
	s_or_b64 exec, exec, s[38:39]
	v_lshlrev_b32_e32 v41, 2, v204
	v_and_b32_e32 v41, 28, v41
	global_load_dword v30, v41, s[10:11] sc1
	v_lshrrev_b32_e32 v202, 4, v204
	v_and_b32_e32 v31, 15, v204
	v_xor_b32_e32 v32, v31, v202
	v_xor_b32_e32 v33, 4, v32
	v_lshlrev_b32_e32 v34, 8, v202
	v_or_b32_e32 v35, 0x10000, v40
	v_add_u32_e32 v34, v34, v35
	v_lshl_add_u32 v24, v32, 4, v34
	v_lshl_add_u32 v25, v33, 4, v34
	v_pk_mul_f32 v[138:139], v[138:139], s[44:45] op_sel_hi:[1,0]
	v_pk_mul_f32 v[140:141], v[140:141], s[44:45] op_sel_hi:[1,0]
	v_pk_mul_f32 v[142:143], v[142:143], s[44:45] op_sel_hi:[1,0]
	v_pk_mul_f32 v[144:145], v[144:145], s[44:45] op_sel_hi:[1,0]
	v_cvt_pk_bf16_f32 v12, v138, v139
	v_cvt_pk_bf16_f32 v13, v140, v141
	v_cvt_pk_bf16_f32 v14, v142, v143
	v_cvt_pk_bf16_f32 v15, v144, v145
	ds_write_b128 v24, v[12:15] offset:0
	v_pk_mul_f32 v[146:147], v[146:147], s[44:45] op_sel_hi:[1,0]
	v_pk_mul_f32 v[148:149], v[148:149], s[44:45] op_sel_hi:[1,0]
	v_pk_mul_f32 v[150:151], v[150:151], s[44:45] op_sel_hi:[1,0]
	v_pk_mul_f32 v[152:153], v[152:153], s[44:45] op_sel_hi:[1,0]
	v_cvt_pk_bf16_f32 v16, v146, v147
	v_cvt_pk_bf16_f32 v17, v148, v149
	v_cvt_pk_bf16_f32 v18, v150, v151
	v_cvt_pk_bf16_f32 v19, v152, v153
	ds_write_b128 v25, v[16:19] offset:1024
	v_pk_mul_f32 v[154:155], v[154:155], s[44:45] op_sel_hi:[1,0]
	v_pk_mul_f32 v[156:157], v[156:157], s[44:45] op_sel_hi:[1,0]
	v_pk_mul_f32 v[158:159], v[158:159], s[44:45] op_sel_hi:[1,0]
	v_pk_mul_f32 v[160:161], v[160:161], s[44:45] op_sel_hi:[1,0]
	v_cvt_pk_bf16_f32 v20, v154, v155
	v_cvt_pk_bf16_f32 v21, v156, v157
	v_cvt_pk_bf16_f32 v22, v158, v159
	v_cvt_pk_bf16_f32 v23, v160, v161
	ds_write_b128 v24, v[20:23] offset:2048
	v_pk_mul_f32 v[162:163], v[162:163], s[44:45] op_sel_hi:[1,0]
	v_pk_mul_f32 v[164:165], v[164:165], s[44:45] op_sel_hi:[1,0]
	v_pk_mul_f32 v[166:167], v[166:167], s[44:45] op_sel_hi:[1,0]
	v_pk_mul_f32 v[168:169], v[168:169], s[44:45] op_sel_hi:[1,0]
	v_cvt_pk_bf16_f32 v12, v162, v163
	v_cvt_pk_bf16_f32 v13, v164, v165
	v_cvt_pk_bf16_f32 v14, v166, v167
	v_cvt_pk_bf16_f32 v15, v168, v169
	ds_write_b128 v25, v[12:15] offset:3072
	v_pk_mul_f32 v[170:171], v[170:171], s[44:45] op_sel_hi:[1,0]
	v_pk_mul_f32 v[172:173], v[172:173], s[44:45] op_sel_hi:[1,0]
	v_pk_mul_f32 v[174:175], v[174:175], s[44:45] op_sel_hi:[1,0]
	v_pk_mul_f32 v[176:177], v[176:177], s[44:45] op_sel_hi:[1,0]
	v_cvt_pk_bf16_f32 v16, v170, v171
	v_cvt_pk_bf16_f32 v17, v172, v173
	v_cvt_pk_bf16_f32 v18, v174, v175
	v_cvt_pk_bf16_f32 v19, v176, v177
	ds_write_b128 v24, v[16:19] offset:4096
	v_pk_mul_f32 v[178:179], v[178:179], s[44:45] op_sel_hi:[1,0]
	v_pk_mul_f32 v[180:181], v[180:181], s[44:45] op_sel_hi:[1,0]
	v_pk_mul_f32 v[182:183], v[182:183], s[44:45] op_sel_hi:[1,0]
	v_pk_mul_f32 v[184:185], v[184:185], s[44:45] op_sel_hi:[1,0]
	v_cvt_pk_bf16_f32 v20, v178, v179
	v_cvt_pk_bf16_f32 v21, v180, v181
	v_cvt_pk_bf16_f32 v22, v182, v183
	v_cvt_pk_bf16_f32 v23, v184, v185
	ds_write_b128 v25, v[20:23] offset:5120
	v_pk_mul_f32 v[186:187], v[186:187], s[44:45] op_sel_hi:[1,0]
	v_pk_mul_f32 v[188:189], v[188:189], s[44:45] op_sel_hi:[1,0]
	v_pk_mul_f32 v[190:191], v[190:191], s[44:45] op_sel_hi:[1,0]
	v_pk_mul_f32 v[192:193], v[192:193], s[44:45] op_sel_hi:[1,0]
	v_cvt_pk_bf16_f32 v12, v186, v187
	v_cvt_pk_bf16_f32 v13, v188, v189
	v_cvt_pk_bf16_f32 v14, v190, v191
	v_cvt_pk_bf16_f32 v15, v192, v193
	ds_write_b128 v24, v[12:15] offset:6144
	v_pk_mul_f32 v[194:195], v[194:195], s[44:45] op_sel_hi:[1,0]
	v_pk_mul_f32 v[196:197], v[196:197], s[44:45] op_sel_hi:[1,0]
	v_pk_mul_f32 v[198:199], v[198:199], s[44:45] op_sel_hi:[1,0]
	v_pk_mul_f32 v[200:201], v[200:201], s[44:45] op_sel_hi:[1,0]
	v_cvt_pk_bf16_f32 v16, v194, v195
	v_cvt_pk_bf16_f32 v17, v196, v197
	v_cvt_pk_bf16_f32 v18, v198, v199
	v_cvt_pk_bf16_f32 v19, v200, v201
	ds_write_b128 v25, v[16:19] offset:7168
	v_pk_mul_f32 v[42:43], v[42:43], s[44:45] op_sel_hi:[1,0]
	v_pk_mul_f32 v[44:45], v[44:45], s[44:45] op_sel_hi:[1,0]
	v_pk_mul_f32 v[46:47], v[46:47], s[44:45] op_sel_hi:[1,0]
	v_pk_mul_f32 v[48:49], v[48:49], s[44:45] op_sel_hi:[1,0]
	v_cvt_pk_bf16_f32 v20, v42, v43
	v_cvt_pk_bf16_f32 v21, v44, v45
	v_cvt_pk_bf16_f32 v22, v46, v47
	v_cvt_pk_bf16_f32 v23, v48, v49
	ds_write_b128 v24, v[20:23] offset:8192
	v_pk_mul_f32 v[50:51], v[50:51], s[44:45] op_sel_hi:[1,0]
	v_pk_mul_f32 v[52:53], v[52:53], s[44:45] op_sel_hi:[1,0]
	v_pk_mul_f32 v[54:55], v[54:55], s[44:45] op_sel_hi:[1,0]
	v_pk_mul_f32 v[56:57], v[56:57], s[44:45] op_sel_hi:[1,0]
	v_cvt_pk_bf16_f32 v12, v50, v51
	v_cvt_pk_bf16_f32 v13, v52, v53
	v_cvt_pk_bf16_f32 v14, v54, v55
	v_cvt_pk_bf16_f32 v15, v56, v57
	ds_write_b128 v25, v[12:15] offset:9216
	v_pk_mul_f32 v[58:59], v[58:59], s[44:45] op_sel_hi:[1,0]
	v_pk_mul_f32 v[60:61], v[60:61], s[44:45] op_sel_hi:[1,0]
	v_pk_mul_f32 v[62:63], v[62:63], s[44:45] op_sel_hi:[1,0]
	v_pk_mul_f32 v[64:65], v[64:65], s[44:45] op_sel_hi:[1,0]
	v_cvt_pk_bf16_f32 v16, v58, v59
	v_cvt_pk_bf16_f32 v17, v60, v61
	v_cvt_pk_bf16_f32 v18, v62, v63
	v_cvt_pk_bf16_f32 v19, v64, v65
	ds_write_b128 v24, v[16:19] offset:10240
	v_pk_mul_f32 v[66:67], v[66:67], s[44:45] op_sel_hi:[1,0]
	v_pk_mul_f32 v[68:69], v[68:69], s[44:45] op_sel_hi:[1,0]
	v_pk_mul_f32 v[70:71], v[70:71], s[44:45] op_sel_hi:[1,0]
	v_pk_mul_f32 v[72:73], v[72:73], s[44:45] op_sel_hi:[1,0]
	v_cvt_pk_bf16_f32 v20, v66, v67
	v_cvt_pk_bf16_f32 v21, v68, v69
	v_cvt_pk_bf16_f32 v22, v70, v71
	v_cvt_pk_bf16_f32 v23, v72, v73
	ds_write_b128 v25, v[20:23] offset:11264
	v_pk_mul_f32 v[74:75], v[74:75], s[44:45] op_sel_hi:[1,0]
	v_pk_mul_f32 v[76:77], v[76:77], s[44:45] op_sel_hi:[1,0]
	v_pk_mul_f32 v[78:79], v[78:79], s[44:45] op_sel_hi:[1,0]
	v_pk_mul_f32 v[80:81], v[80:81], s[44:45] op_sel_hi:[1,0]
	v_cvt_pk_bf16_f32 v12, v74, v75
	v_cvt_pk_bf16_f32 v13, v76, v77
	v_cvt_pk_bf16_f32 v14, v78, v79
	v_cvt_pk_bf16_f32 v15, v80, v81
	ds_write_b128 v24, v[12:15] offset:12288
	v_pk_mul_f32 v[82:83], v[82:83], s[44:45] op_sel_hi:[1,0]
	v_pk_mul_f32 v[84:85], v[84:85], s[44:45] op_sel_hi:[1,0]
	v_pk_mul_f32 v[86:87], v[86:87], s[44:45] op_sel_hi:[1,0]
	v_pk_mul_f32 v[88:89], v[88:89], s[44:45] op_sel_hi:[1,0]
	v_cvt_pk_bf16_f32 v16, v82, v83
	v_cvt_pk_bf16_f32 v17, v84, v85
	v_cvt_pk_bf16_f32 v18, v86, v87
	v_cvt_pk_bf16_f32 v19, v88, v89
	ds_write_b128 v25, v[16:19] offset:13312
	v_pk_mul_f32 v[90:91], v[90:91], s[44:45] op_sel_hi:[1,0]
	v_pk_mul_f32 v[92:93], v[92:93], s[44:45] op_sel_hi:[1,0]
	v_pk_mul_f32 v[94:95], v[94:95], s[44:45] op_sel_hi:[1,0]
	v_pk_mul_f32 v[96:97], v[96:97], s[44:45] op_sel_hi:[1,0]
	v_cvt_pk_bf16_f32 v20, v90, v91
	v_cvt_pk_bf16_f32 v21, v92, v93
	v_cvt_pk_bf16_f32 v22, v94, v95
	v_cvt_pk_bf16_f32 v23, v96, v97
	ds_write_b128 v24, v[20:23] offset:14336
	v_pk_mul_f32 v[98:99], v[98:99], s[44:45] op_sel_hi:[1,0]
	v_pk_mul_f32 v[100:101], v[100:101], s[44:45] op_sel_hi:[1,0]
	v_pk_mul_f32 v[102:103], v[102:103], s[44:45] op_sel_hi:[1,0]
	v_pk_mul_f32 v[104:105], v[104:105], s[44:45] op_sel_hi:[1,0]
	v_cvt_pk_bf16_f32 v12, v98, v99
	v_cvt_pk_bf16_f32 v13, v100, v101
	v_cvt_pk_bf16_f32 v14, v102, v103
	v_cvt_pk_bf16_f32 v15, v104, v105
	ds_write_b128 v25, v[12:15] offset:15360
	v_and_b32_e32 v200, 0xc0, v0
	v_add_u32_e32 v200, s31, v200
	v_add_u32_e32 v200, s24, v200
	v_mov_b32_e32 v201, v35
	v_add_u32_e32 v203, 4, v202
	v_add_u32_e32 v205, 8, v202
	v_add_u32_e32 v206, 12, v202
	v_add_u32_e32 v207, 16, v202
	v_add_u32_e32 v208, 20, v202
	v_add_u32_e32 v209, 24, v202
	v_add_u32_e32 v210, 28, v202
	s_mov_b32 s22, 0x600df1a6
	s_mov_b32 s23, 0x10000
	s_waitcnt vmcnt(0) lgkmcnt(0)
	v_cmp_eq_u32_e32 vcc, s22, v30
	s_cmp_eq_u64 vcc, exec
	s_cbranch_scc0 .LBB0_27
